# baseline (speedup 1.0000x reference)
_Z16bilateral_kernelPKfS0_Pf:
	s_load_dwordx2 s[4:5], s[0:1], 0x0
	s_load_dwordx2 s[8:9], s[0:1], 0x10
	s_lshr_b32 s19, s2, 8
	s_and_b32 s0, s2, 7
	s_mulk_i32 s0, 0x60
	s_lshr_b32 s1, s2, 3
	s_add_i32 s1, s0, s1
	s_lshr_b32 s0, s1, 6
	s_lshl_b32 s11, s1, 6
	s_nop 0
	s_and_b32 s11, s11, 0x1c0
	s_lshl_b32 s1, s1, 3
	s_nop 0
	s_and_b32 s10, s1, 0x1c0
	s_mov_b32 s1, 0
	s_lshl_b64 s[2:3], s[0:1], 20
	s_mov_b32 s20, 0xc05dfbe6
	s_mov_b32 s21, 0xc05dfbe6
	s_mov_b32 s22, 0xc0a8390e
	s_mov_b32 s23, 0xc0a8390e
	s_mov_b32 s24, 0xc08211a7
	s_mov_b32 s25, 0xc08211a7
	s_mov_b32 s26, 0xc0bb4cc1
	s_mov_b32 s27, 0xc0bb4cc1
	s_mov_b32 s28, 0xc0f487dc
	s_mov_b32 s29, 0xc0f487dc
	s_mov_b32 s30, 0x3e0bd796
	s_mov_b32 s31, 0x3e0bd796
	s_mov_b32 s32, 0x3f45a90c
	s_mov_b32 s33, 0x3f45a90c
	s_mov_b32 s34, 0x3fa5c782
	s_mov_b32 s35, 0x3fa5c782
	v_and_b32_e32 v118, 15, v0
	v_lshrrev_b32_e32 v115, 2, v0
	v_lshl_or_b32 v113, v118, 2, s11
	v_and_or_b32 v117, v115, 60, s10
	v_min_u32_e32 v116, 0x1fa, v113
	v_sub_u32_e64 v115, v113, 2 clamp
	v_add_u32_e64 v116, 4, v116
	v_cmp_eq_u32_e64 s[16:17], 0, v118
	v_cmp_eq_u32_e32 vcc, 15, v118
	s_nop 1
	v_cndmask_b32_e64 v115, v116, v115, s[16:17]
	s_or_b64 vcc, s[16:17], vcc
	v_lshlrev_b32_e32 v115, 2, v115
	v_mov_b32_e32 v116, 0x7ff00000
	s_nop 0
	v_cndmask_b32_e32 v112, v116, v115, vcc
	s_movk_i32 s18, 0x1fc
	v_cmp_eq_u32_e32 vcc, 0, v113
	v_cmp_eq_u32_e64 s[16:17], s18, v113
	v_lshlrev_b32_e32 v113, 2, v113
	s_waitcnt lgkmcnt(0)
	s_add_u32 s4, s4, s2
	s_addc_u32 s5, s5, s3
	s_and_b32 s5, s5, 0xffff
	s_mov_b32 s6, 0x100000
	s_mov_b32 s7, 0x20000
	s_add_u32 s12, s8, s2
	s_addc_u32 s13, s9, s3
	s_and_b32 s13, s13, 0xffff
	s_mov_b32 s14, 0x100000
	s_mov_b32 s15, 0x20000
	s_cmp_eq_u32 s19, 0
	s_cbranch_scc1 .Lmynosl
	s_sleep 2
	s_cmp_eq_u32 s19, 1
	s_cbranch_scc1 .Lmynosl
	s_sleep 2
